# P11 shared rope-key loop: four iterations per round, all 16 loads issued before one wait, then the four compute+store groups under saved exec masks (was load-wait-store per iteration)
# baseline (speedup 1.0000x reference)
; __device__ __forceinline__ float bf2f(bf16 v) { return __uint_as_float(((unsigned)v) << 16); }
; __device__ __forceinline__ bf16 f2bf(float f) { unsigned u = __float_as_uint(f); return (bf16)((u + 0x7fffu + ((u >> 16) & 1u)) >> 16); }
; template <int PH>
; __device__ __forceinline__ void mk_body(const Args& a) {
;     ...
;         for (int it = bid * NTHR + tid; it < M * 16; it += G * NTHR) {
;             const int m = it >> 4, i = it & 15, t = m & (S - 1);
;             const float x1 = bf2f(y1[(size_t)m * Y1P + Y1_MKR + i]), x2 = bf2f(y1[(size_t)m * Y1P + Y1_MKR + 16 + i]);
;             const float cs = rope_cos[t * 16 + i], sn = rope_sin[t * 16 + i];
;             krope[(size_t)m * 32 + i] = f2bf(x1 * cs - x2 * sn);
;             krope[(size_t)m * 32 + 16 + i] = f2bf(x2 * cs + x1 * sn);
;         }
.LBB0_2311:
	s_mov_b64 s[12:13], exec
	v_ashrrev_i32_e32 v6, 4, v4
	v_ashrrev_i32_e32 v7, 31, v6
	v_lshlrev_b64 v[8:9], 12, v[6:7]
	v_and_b32_e32 v5, 0x1ffff, v4
	v_lshl_add_u64 v[8:9], v[2:3], 0, v[8:9]
	v_lshlrev_b32_e32 v5, 2, v5
	global_load_ushort v10, v[8:9], off offset:3840
	global_load_ushort v11, v[8:9], off offset:3872
	global_load_dword v12, v5, s[6:7]
	global_load_dword v13, v5, s[4:5]
	v_lshlrev_b64 v[6:7], 6, v[6:7]
	v_lshl_add_u64 v[6:7], v[0:1], 0, v[6:7]
	v_add_u32_e32 v4, s0, v4
	v_cmp_ge_i32_e32 vcc, s10, v4
	s_and_b64 exec, exec, vcc
	s_mov_b64 s[14:15], exec
	v_ashrrev_i32_e32 v16, 4, v4
	v_ashrrev_i32_e32 v17, 31, v16
	v_lshlrev_b64 v[18:19], 12, v[16:17]
	v_and_b32_e32 v20, 0x1ffff, v4
	v_lshl_add_u64 v[18:19], v[2:3], 0, v[18:19]
	v_lshlrev_b32_e32 v20, 2, v20
	global_load_ushort v21, v[18:19], off offset:3840
	global_load_ushort v22, v[18:19], off offset:3872
	global_load_dword v23, v20, s[6:7]
	global_load_dword v24, v20, s[4:5]
	v_lshlrev_b64 v[16:17], 6, v[16:17]
	v_lshl_add_u64 v[16:17], v[0:1], 0, v[16:17]
	v_add_u32_e32 v4, s0, v4
	v_cmp_ge_i32_e32 vcc, s10, v4
	s_and_b64 exec, exec, vcc
	s_mov_b64 s[16:17], exec
	v_ashrrev_i32_e32 v28, 4, v4
	v_ashrrev_i32_e32 v29, 31, v28
	v_lshlrev_b64 v[30:31], 12, v[28:29]
	v_and_b32_e32 v32, 0x1ffff, v4
	v_lshl_add_u64 v[30:31], v[2:3], 0, v[30:31]
	v_lshlrev_b32_e32 v32, 2, v32
	global_load_ushort v33, v[30:31], off offset:3840
	global_load_ushort v34, v[30:31], off offset:3872
	global_load_dword v35, v32, s[6:7]
	global_load_dword v36, v32, s[4:5]
	v_lshlrev_b64 v[28:29], 6, v[28:29]
	v_lshl_add_u64 v[28:29], v[0:1], 0, v[28:29]
	v_add_u32_e32 v4, s0, v4
	v_cmp_ge_i32_e32 vcc, s10, v4
	s_and_b64 exec, exec, vcc
	s_mov_b64 s[18:19], exec
	v_ashrrev_i32_e32 v40, 4, v4
	v_ashrrev_i32_e32 v41, 31, v40
	v_lshlrev_b64 v[42:43], 12, v[40:41]
	v_and_b32_e32 v44, 0x1ffff, v4
	v_lshl_add_u64 v[42:43], v[2:3], 0, v[42:43]
	v_lshlrev_b32_e32 v44, 2, v44
	global_load_ushort v45, v[42:43], off offset:3840
	global_load_ushort v46, v[42:43], off offset:3872
	global_load_dword v47, v44, s[6:7]
	global_load_dword v48, v44, s[4:5]
	v_lshlrev_b64 v[40:41], 6, v[40:41]
	v_lshl_add_u64 v[40:41], v[0:1], 0, v[40:41]
	v_add_u32_e32 v4, s0, v4
	v_cmp_ge_i32_e32 vcc, s10, v4
	s_and_b64 exec, exec, vcc
	s_mov_b64 s[20:21], exec
	s_mov_b64 exec, s[12:13]
	s_waitcnt vmcnt(0)
	v_lshlrev_b32_e32 v5, 16, v10
	v_lshlrev_b32_e32 v8, 16, v11
	v_mul_f32_e32 v9, v12, v8
	v_mul_f32_e32 v8, v13, v8
	v_fma_f32 v9, v13, v5, -v9
	v_fmac_f32_e32 v8, v12, v5
	v_bfe_u32 v5, v9, 16, 1
	v_bfe_u32 v10, v8, 16, 1
	v_add3_u32 v5, v9, v5, s1
	v_add3_u32 v8, v8, v10, s1
	global_store_short_d16_hi v[6:7], v5, off
	global_store_short_d16_hi v[6:7], v8, off offset:32
	s_mov_b64 exec, s[14:15]
	v_lshlrev_b32_e32 v20, 16, v21
	v_lshlrev_b32_e32 v18, 16, v22
	v_mul_f32_e32 v19, v23, v18
	v_mul_f32_e32 v18, v24, v18
	v_fma_f32 v19, v24, v20, -v19
	v_fmac_f32_e32 v18, v23, v20
	v_bfe_u32 v20, v19, 16, 1
	v_bfe_u32 v21, v18, 16, 1
	v_add3_u32 v20, v19, v20, s1
	v_add3_u32 v18, v18, v21, s1
	global_store_short_d16_hi v[16:17], v20, off
	global_store_short_d16_hi v[16:17], v18, off offset:32
	s_mov_b64 exec, s[16:17]
	v_lshlrev_b32_e32 v32, 16, v33
	v_lshlrev_b32_e32 v30, 16, v34
	v_mul_f32_e32 v31, v35, v30
	v_mul_f32_e32 v30, v36, v30
	v_fma_f32 v31, v36, v32, -v31
	v_fmac_f32_e32 v30, v35, v32
	v_bfe_u32 v32, v31, 16, 1
	v_bfe_u32 v33, v30, 16, 1
	v_add3_u32 v32, v31, v32, s1
	v_add3_u32 v30, v30, v33, s1
	global_store_short_d16_hi v[28:29], v32, off
	global_store_short_d16_hi v[28:29], v30, off offset:32
	s_mov_b64 exec, s[18:19]
	v_lshlrev_b32_e32 v44, 16, v45
	v_lshlrev_b32_e32 v42, 16, v46
	v_mul_f32_e32 v43, v47, v42
	v_mul_f32_e32 v42, v48, v42
	v_fma_f32 v43, v48, v44, -v43
	v_fmac_f32_e32 v42, v47, v44
	v_bfe_u32 v44, v43, 16, 1
	v_bfe_u32 v45, v42, 16, 1
	v_add3_u32 v44, v43, v44, s1
	v_add3_u32 v42, v42, v45, s1
	global_store_short_d16_hi v[40:41], v44, off
	global_store_short_d16_hi v[40:41], v42, off offset:32
	s_mov_b64 exec, s[20:21]
	s_cbranch_execnz .LBB0_2311
